# prologue bf16 row stores carry the non-temporal hint (less dirty L2 data to write back at barrier 0)
# baseline (speedup 1.0000x reference)
; #define GAS __attribute__((address_space(1)))
; __device__ __forceinline__ unsigned pk2(float lo, float hi) { return f2bf(lo) | (f2bf(hi) << 16); }
; __device__ __forceinline__ void p0_prologue(const Frame& F) {
;     ...
;         for (int m = rw; m < M; m += 2 * NRW) {
;             const int m2 = m + NRW; const bool two = m2 < M;
;             const GAS f32x4* xr = (const GAS f32x4*)(x + (size_t)m * D) + F.lane; const GAS f32x4* xr2 = (const GAS f32x4*)(x + (size_t)(two ? m2 : m) * D) + F.lane; f32x4 v[4], v2[4]; float s = 0.f, s2 = 0.f;
; #pragma unroll
;             for (int j = 0; j < 4; ++j) { v[j] = __builtin_nontemporal_load(&xr[64 * j]); v2[j] = __builtin_nontemporal_load(&xr2[64 * j]); }
; #pragma unroll
;             for (int j = 0; j < 4; ++j) { s += (v[j][0] * v[j][0] + v[j][1] * v[j][1]) + (v[j][2] * v[j][2] + v[j][3] * v[j][3]); s2 += (v2[j][0] * v2[j][0] + v2[j][1] * v2[j][1]) + (v2[j][2] * v2[j][2] + v2[j][3] * v2[j][3]); }
;             s = wave_sum(s); s2 = wave_sum(s2);
;             GAS unsigned long long* o8 = (GAS unsigned long long*)(xb + (size_t)m * D) + F.lane;
; #pragma unroll
;             for (int j = 0; j < 4; ++j) o8[64 * j] = (unsigned long long)pk2(v[j][0], v[j][1]) | ((unsigned long long)pk2(v[j][2], v[j][3]) << 32);
;             if (F.lane < 16) ssp[(size_t)m * 16 + F.lane] = (F.lane == 0) ? s : 0.f;
;             if (two) { GAS unsigned long long* o82 = (GAS unsigned long long*)(xb + (size_t)m2 * D) + F.lane;
; #pragma unroll
;                 for (int j = 0; j < 4; ++j) o82[64 * j] = (unsigned long long)pk2(v2[j][0], v2[j][1]) | ((unsigned long long)pk2(v2[j][2], v2[j][3]) << 32);
;                 if (F.lane < 16) ssp[(size_t)m2 * 16 + F.lane] = (F.lane == 0) ? s2 : 0.f; }
.LBB0_156:
	s_add_i32 s20, s2, s16
	s_cmpk_lt_i32 s20, 0x4000
	s_cselect_b64 s[22:23], -1, 0
	s_waitcnt lgkmcnt(0)
	global_load_dwordx4 v[38:41], v[30:31], off offset:-2048 nt
	global_load_dwordx4 v[42:45], v[30:31], off offset:-1024 nt
	global_load_dwordx4 v[46:49], v[30:31], off nt
	global_load_dwordx4 v[16:19], v[30:31], off offset:1024 nt
	s_and_b64 s[24:25], s[22:23], exec
	s_cselect_b32 s24, s20, s16
	s_ashr_i32 s25, s24, 31
	s_lshl_b64 s[24:25], s[24:25], 12
	v_lshl_add_u64 v[50:51], v[20:21], 0, s[24:25]
	global_load_dwordx4 v[12:15], v[50:51], off nt
	global_load_dwordx4 v[8:11], v[50:51], off offset:1024 nt
	global_load_dwordx4 v[4:7], v[50:51], off offset:2048 nt
	global_load_dwordx4 v[0:3], v[50:51], off offset:3072 nt
	v_lshl_add_u64 v[50:51], s[14:15], 0, v[28:29]
	v_add_co_u32_e32 v50, vcc, s17, v50
	s_waitcnt vmcnt(7)
	v_mul_f32_e32 v52, v39, v39
	v_mul_f32_e32 v53, v41, v41
	s_waitcnt vmcnt(6)
	v_mul_f32_e32 v54, v43, v43
	v_mul_f32_e32 v55, v45, v45
	s_waitcnt vmcnt(5)
	v_mul_f32_e32 v56, v47, v47
	v_mul_f32_e32 v57, v49, v49
	v_fmac_f32_e32 v52, v38, v38
	v_fmac_f32_e32 v53, v40, v40
	v_fmac_f32_e32 v54, v42, v42
	v_fmac_f32_e32 v55, v44, v44
	s_waitcnt vmcnt(4)
	v_mul_f32_e32 v58, v17, v17
	v_mul_f32_e32 v59, v19, v19
	v_fmac_f32_e32 v56, v46, v46
	v_fmac_f32_e32 v57, v48, v48
	v_add_f32_e32 v52, v52, v53
	v_add_f32_e32 v53, v54, v55
	v_fmac_f32_e32 v58, v16, v16
	v_fmac_f32_e32 v59, v18, v18
	v_add_f32_e32 v54, v56, v57
	v_add_f32_e32 v52, v52, v53
	v_add_f32_e32 v55, v58, v59
	v_add_f32_e32 v52, v52, v54
	v_add_f32_e32 v52, v52, v55
	s_waitcnt vmcnt(3)
	v_mul_f32_e32 v54, v13, v13
	v_mul_f32_e32 v55, v15, v15
	s_waitcnt vmcnt(2)
	v_mul_f32_e32 v56, v9, v9
	v_mul_f32_e32 v57, v11, v11
	v_bfe_u32 v60, v38, 16, 1
	v_bfe_u32 v61, v39, 16, 1
	s_waitcnt vmcnt(1)
	v_mul_f32_e32 v58, v5, v5
	v_mul_f32_e32 v59, v7, v7
	v_fmac_f32_e32 v54, v12, v12
	v_fmac_f32_e32 v55, v14, v14
	v_fmac_f32_e32 v56, v8, v8
	v_fmac_f32_e32 v57, v10, v10
	v_add3_u32 v38, v38, v60, s3
	v_add3_u32 v39, v39, v61, s3
	s_waitcnt vmcnt(0)
	v_mul_f32_e32 v60, v1, v1
	v_mul_f32_e32 v61, v3, v3
	v_fmac_f32_e32 v58, v4, v4
	v_fmac_f32_e32 v59, v6, v6
	v_add_f32_e32 v54, v54, v55
	v_add_f32_e32 v55, v56, v57
	ds_bpermute_b32 v53, v32, v52
	v_fmac_f32_e32 v60, v0, v0
	v_fmac_f32_e32 v61, v2, v2
	v_add_f32_e32 v56, v58, v59
	v_add_f32_e32 v54, v54, v55
	v_add_f32_e32 v57, v60, v61
	v_add_f32_e32 v54, v54, v56
	v_add_f32_e32 v54, v54, v57
	ds_bpermute_b32 v55, v32, v54
	s_waitcnt lgkmcnt(1)
	v_add_f32_e32 v52, v52, v53
	ds_bpermute_b32 v53, v33, v52
	v_bfe_u32 v62, v40, 16, 1
	v_bfe_u32 v64, v42, 16, 1
	s_waitcnt lgkmcnt(1)
	v_add_f32_e32 v54, v54, v55
	ds_bpermute_b32 v55, v33, v54
	s_waitcnt lgkmcnt(1)
	v_add_f32_e32 v52, v52, v53
	ds_bpermute_b32 v53, v34, v52
	v_bfe_u32 v63, v41, 16, 1
	v_bfe_u32 v65, v43, 16, 1
	s_waitcnt lgkmcnt(1)
	v_add_f32_e32 v54, v54, v55
	v_add3_u32 v40, v40, v62, s3
	v_add3_u32 v42, v42, v64, s3
	ds_bpermute_b32 v55, v34, v54
	v_add3_u32 v41, v41, v63, s3
	v_add3_u32 v43, v43, v65, s3
	v_lshrrev_b32_e32 v38, 16, v38
	v_lshrrev_b32_e32 v40, 16, v40
	v_lshrrev_b32_e32 v42, 16, v42
	v_and_or_b32 v38, v39, s9, v38
	v_and_or_b32 v39, v41, s9, v40
	v_and_or_b32 v40, v43, s9, v42
	s_waitcnt lgkmcnt(1)
	v_add_f32_e32 v43, v52, v53
	ds_bpermute_b32 v52, v35, v43
	s_waitcnt lgkmcnt(1)
	v_add_f32_e32 v53, v54, v55
	v_bfe_u32 v66, v44, 16, 1
	ds_bpermute_b32 v54, v35, v53
	v_bfe_u32 v67, v45, 16, 1
	v_add3_u32 v44, v44, v66, s3
	v_add3_u32 v45, v45, v67, s3
	v_lshrrev_b32_e32 v44, 16, v44
	s_waitcnt lgkmcnt(1)
	v_add_f32_e32 v43, v43, v52
	v_bfe_u32 v68, v46, 16, 1
	v_and_or_b32 v41, v45, s9, v44
	ds_bpermute_b32 v44, v36, v43
	v_bfe_u32 v69, v47, 16, 1
	v_add3_u32 v46, v46, v68, s3
	v_add3_u32 v47, v47, v69, s3
	v_lshrrev_b32_e32 v46, 16, v46
	s_waitcnt lgkmcnt(1)
	v_add_f32_e32 v45, v53, v54
	v_bfe_u32 v70, v48, 16, 1
	v_and_or_b32 v42, v47, s9, v46
	ds_bpermute_b32 v46, v36, v45
	v_addc_co_u32_e32 v51, vcc, 0, v51, vcc
	v_bfe_u32 v71, v49, 16, 1
	v_add3_u32 v48, v48, v70, s3
	v_lshrrev_b32_e32 v48, 16, v48
	global_store_dwordx2 v[50:51], v[38:39], off nt
	global_store_dwordx2 v[50:51], v[40:41], off offset:512 nt
	s_waitcnt lgkmcnt(1)
	v_add_f32_e32 v40, v43, v44
	v_add3_u32 v43, v49, v71, s3
	v_and_or_b32 v43, v43, s9, v48
	global_store_dwordx2 v[50:51], v[42:43], off offset:1024 nt
	v_bfe_u32 v42, v16, 16, 1
	s_waitcnt lgkmcnt(0)
	v_add_f32_e32 v38, v45, v46
	v_add3_u32 v16, v16, v42, s3
	v_bfe_u32 v42, v17, 16, 1
	ds_bpermute_b32 v41, v37, v40
	ds_bpermute_b32 v39, v37, v38
	v_lshrrev_b32_e32 v16, 16, v16
	v_add3_u32 v17, v17, v42, s3
	v_and_or_b32 v16, v17, s9, v16
	v_bfe_u32 v17, v18, 16, 1
	v_add3_u32 v17, v18, v17, s3
	v_bfe_u32 v18, v19, 16, 1
	v_lshrrev_b32_e32 v17, 16, v17
	v_add3_u32 v18, v19, v18, s3
	v_and_or_b32 v17, v18, s9, v17
	global_store_dwordx2 v[50:51], v[16:17], off offset:1536 nt
	s_and_saveexec_b64 s[24:25], s[4:5]
	s_cbranch_execz .LBB0_158
	s_waitcnt lgkmcnt(1)
	v_add_f32_e32 v16, v40, v41
	v_cndmask_b32_e64 v18, 0, v16, s[6:7]
	v_lshl_add_u64 v[16:17], s[14:15], 0, v[26:27]
	global_store_dword v[16:17], v18, off
; #define GAS __attribute__((address_space(1)))
; __device__ __forceinline__ unsigned pk2(float lo, float hi) { return f2bf(lo) | (f2bf(hi) << 16); }
; __device__ __forceinline__ void p0_prologue(const Frame& F) {
;     ...
;             if (two) { GAS unsigned long long* o82 = (GAS unsigned long long*)(xb + (size_t)m2 * D) + F.lane;
; #pragma unroll
;                 for (int j = 0; j < 4; ++j) o82[64 * j] = (unsigned long long)pk2(v2[j][0], v2[j][1]) | ((unsigned long long)pk2(v2[j][2], v2[j][3]) << 32);
;                 if (F.lane < 16) ssp[(size_t)m2 * 16 + F.lane] = (F.lane == 0) ? s2 : 0.f; }
.LBB0_158:
	s_or_b64 exec, exec, s[24:25]
	s_andn2_b64 vcc, exec, s[22:23]
	s_cbranch_vccnz .LBB0_155
	v_bfe_u32 v18, v12, 16, 1
	v_add3_u32 v12, v12, v18, s3
	v_bfe_u32 v18, v13, 16, 1
	v_lshrrev_b32_e32 v12, 16, v12
	v_add3_u32 v13, v13, v18, s3
	v_and_or_b32 v12, v13, s9, v12
	v_bfe_u32 v13, v14, 16, 1
	s_ashr_i32 s21, s20, 31
	v_add3_u32 v13, v14, v13, s3
	v_bfe_u32 v14, v15, 16, 1
	s_lshl_b64 s[22:23], s[20:21], 11
	v_lshrrev_b32_e32 v13, 16, v13
	v_add3_u32 v14, v15, v14, s3
	v_lshl_add_u64 v[16:17], v[22:23], 0, s[22:23]
	v_and_or_b32 v13, v14, s9, v13
	global_store_dwordx2 v[16:17], v[12:13], off nt
	v_bfe_u32 v12, v8, 16, 1
	v_add3_u32 v8, v8, v12, s3
	v_bfe_u32 v12, v9, 16, 1
	v_lshrrev_b32_e32 v8, 16, v8
	v_add3_u32 v9, v9, v12, s3
	v_and_or_b32 v8, v9, s9, v8
	v_bfe_u32 v9, v10, 16, 1
	v_add3_u32 v9, v10, v9, s3
	v_bfe_u32 v10, v11, 16, 1
	v_lshrrev_b32_e32 v9, 16, v9
	v_add3_u32 v10, v11, v10, s3
	v_and_or_b32 v9, v10, s9, v9
	global_store_dwordx2 v[16:17], v[8:9], off offset:512 nt
	v_bfe_u32 v8, v4, 16, 1
	v_add3_u32 v4, v4, v8, s3
	v_bfe_u32 v8, v5, 16, 1
	v_lshrrev_b32_e32 v4, 16, v4
	v_add3_u32 v5, v5, v8, s3
	v_and_or_b32 v4, v5, s9, v4
	v_bfe_u32 v5, v6, 16, 1
	v_add3_u32 v5, v6, v5, s3
	v_bfe_u32 v6, v7, 16, 1
	v_lshrrev_b32_e32 v5, 16, v5
	v_add3_u32 v6, v7, v6, s3
	v_and_or_b32 v5, v6, s9, v5
	global_store_dwordx2 v[16:17], v[4:5], off offset:1024 nt
	v_bfe_u32 v4, v0, 16, 1
	v_add3_u32 v0, v0, v4, s3
	v_bfe_u32 v4, v1, 16, 1
	v_lshrrev_b32_e32 v0, 16, v0
	v_add3_u32 v1, v1, v4, s3
	v_and_or_b32 v0, v1, s9, v0
	v_bfe_u32 v1, v2, 16, 1
	v_add3_u32 v1, v2, v1, s3
	v_bfe_u32 v2, v3, 16, 1
	v_lshrrev_b32_e32 v1, 16, v1
	v_add3_u32 v2, v3, v2, s3
	v_and_or_b32 v1, v2, s9, v1
	global_store_dwordx2 v[16:17], v[0:1], off offset:1536 nt
	s_and_saveexec_b64 s[22:23], s[4:5]
	s_cbranch_execz .LBB0_154
	s_waitcnt lgkmcnt(0)
	v_add_f32_e32 v0, v38, v39
	s_lshl_b64 s[20:21], s[20:21], 6
	v_cndmask_b32_e64 v2, 0, v0, s[6:7]
	v_lshl_add_u64 v[0:1], v[24:25], 0, s[20:21]
	global_store_dword v[0:1], v2, off
	s_branch .LBB0_154
